# speedup vs baseline: 1.0237x; 1.0068x over previous
_Z8dog_mainPKfS0_S0_S0_S0_S0_S0_Pf:
	s_load_dwordx8 s[12:19], s[0:1], 0x0
	s_load_dwordx8 s[20:27], s[0:1], 0x20
	s_and_b32 s3, s2, 7
	s_lshl_b32 s3, s3, 5
	s_lshr_b32 s4, s2, 3
	s_add_i32 s4, s3, s4
	s_and_b32 s6, s4, 3
	s_lshr_b32 s7, s4, 2
	s_mov_b32 s5, 0
	s_lshl_b64 s[8:9], s[4:5], 18
	v_and_b32_e32 v1, 63, v0
	v_lshrrev_b32_e32 v2, 6, v0
	v_and_b32_e32 v3, 15, v0
	v_and_b32_e32 v7, 31, v0
	v_lshl_or_b32 v5, v2, 5, v7
	v_lshlrev_b32_e32 v5, 2, v5
	v_mov_b32_e32 v4, v5
	v_lshlrev_b32_e32 v6, 4, v1
	v_lshl_or_b32 v6, v2, 12, v6
	v_bfe_u32 v7, v0, 4, 2
	s_waitcnt lgkmcnt(0)
	global_load_dword v32, v4, s[18:19]
	global_load_dword v33, v4, s[20:21]
	global_load_dword v34, v4, s[22:23]
	global_load_dword v35, v4, s[24:25]
	global_load_dword v36, v4, s[14:15]
	global_load_dword v37, v4, s[16:17]
	s_add_u32 s12, s12, s8
	s_addc_u32 s13, s13, s9
	global_load_dwordx4 v[128:131], v6, s[12:13] offset:0 nt
	global_load_dwordx4 v[132:135], v6, s[12:13] offset:1024 nt
	global_load_dwordx4 v[136:139], v6, s[12:13] offset:2048 nt
	global_load_dwordx4 v[140:143], v6, s[12:13] offset:3072 nt
	v_add_u32_e32 v6, 0x8000, v6
	global_load_dwordx4 v[144:147], v6, s[12:13] offset:0 nt
	global_load_dwordx4 v[148:151], v6, s[12:13] offset:1024 nt
	global_load_dwordx4 v[152:155], v6, s[12:13] offset:2048 nt
	global_load_dwordx4 v[156:159], v6, s[12:13] offset:3072 nt
	v_and_b32_e32 v16, 1, v0
	v_cmp_eq_u32_e64 s[30:31], 0, v16
	v_and_b32_e32 v17, 2, v0
	v_cmp_eq_u32_e64 s[32:33], 0, v17
	v_and_b32_e32 v16, 3, v0
	v_lshrrev_b32_e32 v17, 2, v1
	v_lshlrev_b32_e32 v16, 5, v16
	v_lshl_add_u32 v16, v17, 1, v16
	v_lshrrev_b32_e32 v17, 1, v2
	s_movk_i32 s10, 0x110
	v_mad_u32_u24 v16, v17, s10, v16
	v_and_b32_e32 v17, 1, v2
	v_lshl_add_u32 v14, v17, 7, v16
	v_lshlrev_b32_e32 v17, 4, v7
	v_mad_u32_u24 v15, v3, s10, v17
	s_lshl_b32 s11, s6, 5
	v_lshl_add_u32 v18, v7, 2, s11
	v_cvt_f32_u32_e32 v18, v18
	v_lshlrev_b32_e32 v19, 3, v7
	v_cvt_f32_u32_e32 v19, v19
	s_waitcnt vmcnt(8)
	v_lshlrev_b32_e32 v16, 2, v3
	v_add_u32_e32 v17, 64, v16
	ds_bpermute_b32 v40, v16, v32
	ds_bpermute_b32 v46, v17, v32
	ds_bpermute_b32 v41, v16, v33
	ds_bpermute_b32 v47, v17, v33
	ds_bpermute_b32 v42, v16, v34
	ds_bpermute_b32 v48, v17, v34
	ds_bpermute_b32 v43, v16, v35
	ds_bpermute_b32 v49, v17, v35
	ds_bpermute_b32 v44, v16, v36
	ds_bpermute_b32 v50, v17, v36
	ds_bpermute_b32 v45, v16, v37
	ds_bpermute_b32 v51, v17, v37
	s_waitcnt lgkmcnt(0)
	v_add_f32_e32 v41, v40, v41
	v_sub_f32_e32 v12, v19, v42
	v_sub_f32_e32 v13, v18, v43
	v_rcp_f32_e32 v42, v40
	v_rcp_f32_e32 v43, v41
	s_nop 0
	v_fma_f32 v20, -v40, v42, 1.0
	v_fma_f32 v42, v20, v42, v42
	v_fma_f32 v20, -v41, v43, 1.0
	v_fma_f32 v43, v20, v43, v43
	v_mul_f32_e32 v8, 0xbf38aa3b, v42
	v_mul_f32_e32 v9, 0xbf38aa3b, v43
	v_mul_f32_e32 v44, v44, v42
	v_mul_f32_e32 v45, v45, v43
	v_mul_f32_e32 v10, 0x3e22f983, v44
	v_mul_f32_e32 v11, 0x3e22f983, v45
	v_add_f32_e32 v47, v46, v47
	v_sub_f32_e32 v2, v19, v48
	v_sub_f32_e32 v3, v18, v49
	v_rcp_f32_e32 v48, v46
	v_rcp_f32_e32 v49, v47
	s_nop 0
	v_fma_f32 v20, -v46, v48, 1.0
	v_fma_f32 v48, v20, v48, v48
	v_fma_f32 v20, -v47, v49, 1.0
	v_fma_f32 v49, v20, v49, v49
	v_mul_f32_e32 v28, 0xbf38aa3b, v48
	v_mul_f32_e32 v29, 0xbf38aa3b, v49
	v_mul_f32_e32 v50, v50, v48
	v_mul_f32_e32 v51, v51, v49
	v_mul_f32_e32 v30, 0x3e22f983, v50
	v_mul_f32_e32 v31, 0x3e22f983, v51
	s_getpc_b64 s[44:45]
